# v73 with the static priority raise in the differential-attention units given to waves 0-3 instead of 4-7
# baseline (speedup 1.0000x reference)
; DI void attn_unit_d8(unsigned char* lds, const AttnArgs& a) {
;     ...
;     const int lane = tid & 63, r = lane & 31, h = lane >> 5; const int wid = __builtin_amdgcn_readfirstlane(tid >> 6);
;     v8i qfa, qfb;
;     { const bf16_t* qp = a.q + (size_t)(wid * 32 + r) * 256 + 32 * h;
;       const u32x4 q0 = *(const u32x4*)qp, q1 = *(const u32x4*)(qp + 8), q2 = *(const u32x4*)(qp + 16), q3 = *(const u32x4*)(qp + 24);
;       const u32x2 c0 = bf8_to_fp8(q0), c1 = bf8_to_fp8(q1), c2 = bf8_to_fp8(q2), c3 = bf8_to_fp8(q3);
;       const v8i qv = (v8i){(int)c0.x, (int)c0.y, (int)c1.x, (int)c1.y, (int)c2.x, (int)c2.y, (int)c3.x, (int)c3.y}, zz = (v8i){0, 0, 0, 0, 0, 0, 0, 0};
;       qfa = h == 0 ? qv : zz; qfb = h == 1 ? qv : zz; }
;     const int lrow = tid >> 3, lch = tid & 7;
;     const unsigned char* vsrc = a.vt8 + (size_t)lrow * KEYS + 8 * lch;
;     const int ldst = lrow * A8_PITCH + lch * 8;
;     const int ldv = A8_VOFF + lrow * A8_PITCH + (lch >> 2) * 16 + (lch & 3) * 4;
;     const int koff = r * A8_PITCH + 32 * h, voff = A8_VOFF + r * A8_PITCH + 32 * h;
;     f32x16 o0[2], o1[2];
; #pragma unroll
;     for (int d = 0; d < 2; ++d) { o0[d] = (f32x16){}; o1[d] = (f32x16){}; }
;     f32x4 l0 = {0.f, 0.f, 0.f, 0.f}, l1 = {0.f, 0.f, 0.f, 0.f};
;     constexpr int D8_SLOT = 2 * 64 * A8_PITCH;
;     u32x2 kreg0, vreg0, kreg1, vreg1;
;     auto gload = [&](int t, u32x2& kreg, u32x2& vreg) __attribute__((always_inline)) {
;         const unsigned char* kp = (t < 64) ? a.klat8 + (size_t)(t * 64 + lrow) * 256 : a.kctx8 + (size_t)((t - 64) * 64 + lrow) * 256;
;         kreg = *(const u32x2*)(kp + 8 * lch);
;         vreg = *(const u32x2*)(vsrc + (size_t)t * 64);
;     };
;     auto lstore = [&](int slot, const u32x2& kreg, const u32x2& vreg) __attribute__((always_inline)) { unsigned char* b = lds + slot * D8_SLOT;
;         *(u32x2*)(b + ldst) = kreg; *(unsigned*)(b + ldv) = vreg.x; *(unsigned*)(b + ldv + 32) = vreg.y; };
;     auto rd32 = [&](const unsigned char* p) __attribute__((always_inline)) -> v8i { const u32x4 lo = *(const u32x4*)p, hi = *(const u32x4*)(p + 16);
;         return (v8i){(int)lo.x, (int)lo.y, (int)lo.z, (int)lo.w, (int)hi.x, (int)hi.y, (int)hi.z, (int)hi.w}; };
;     auto expsum = [&](f32x16& sc, f32x4& l) __attribute__((always_inline)) {
; #pragma unroll
;         for (int i = 0; i < 16; ++i) sc[i] = __builtin_amdgcn_exp2f(sc[i]);
; #pragma unroll
.LBB0_660:
	s_ashr_i32 s15, s14, 31
	s_lshl_b64 s[48:49], s[14:15], 9
	s_add_u32 s21, s22, s48
	s_addc_u32 s47, s23, s49
	s_lshl_b32 s19, s19, 6
	s_and_b32 s43, s19, 0xc0
	s_lshl_b32 s19, s43, 1
	s_add_u32 s52, s21, s19
	s_addc_u32 s53, s47, 0
	s_ashr_i32 s19, s18, 31
	s_ashr_i32 s21, s20, 31
	s_or_b32 s6, s43, s6
	s_lshl_b64 s[48:49], s[18:19], 8
	s_lshl_b64 s[54:55], s[20:21], 8
	s_mul_hi_i32 s19, s6, 0x1100
	s_mulk_i32 s6, 0x1100
	s_add_u32 s18, s28, s6
	s_addc_u32 s19, s29, s19
	s_add_u32 s6, s24, s48
	s_addc_u32 s21, s25, s49
	s_add_u32 s20, s6, s43
	s_addc_u32 s21, s21, 0
	s_add_u32 s6, s24, s54
	s_addc_u32 s48, s25, s55
	v_mov_b32_e32 v18, v0
	s_add_u32 s47, s6, s43
	s_addc_u32 s48, s48, 0
	v_readfirstlane_b32 s6, v18
	v_and_b32_e32 v30, 31, v18
	s_ashr_i32 s49, s6, 6
	v_lshl_or_b32 v180, s49, 5, v30
	v_ashrrev_i32_e32 v181, 31, v180
	v_bfe_u32 v214, v18, 5, 1
	v_lshlrev_b64 v[2:3], 9, v[180:181]
	v_lshl_add_u64 v[2:3], s[52:53], 0, v[2:3]
	v_lshlrev_b32_e32 v178, 6, v214
	v_lshl_add_u64 v[14:15], v[2:3], 0, v[178:179]
	global_load_dwordx4 v[2:5], v[14:15], off
	global_load_dwordx4 v[6:9], v[14:15], off offset:16
	global_load_dwordx4 v[10:13], v[14:15], off offset:32
	s_nop 0
	global_load_dwordx4 v[14:17], v[14:15], off offset:48
	s_lshl_b32 s6, s46, 6
	v_bfe_i32 v34, v18, 5, 1
	v_ashrrev_i32_e32 v215, 3, v18
	v_and_b32_e32 v35, 7, v18
	v_mov_b64_e32 v[18:19], s[18:19]
	s_add_i32 s52, s6, 0xfffff000
	v_mad_i64_i32 v[18:19], s[18:19], v215, s37, v[18:19]
	s_and_b64 s[18:19], s[16:17], exec
	s_cselect_b32 s52, s6, s52
	s_cselect_b32 s19, s21, s48
	s_cselect_b32 s18, s20, s47
	s_or_b32 s54, s6, 64
	s_add_i32 s55, s6, 0xfffff040
	v_add_u32_e32 v20, s52, v215
	s_and_b64 s[52:53], s[16:17], exec
	v_lshlrev_b32_e32 v178, 3, v35
	s_cselect_b32 s52, s54, s55
	s_or_b32 s53, s6, 0x80
	s_add_i32 s54, s6, 0xfffff080
	v_lshl_add_u64 v[182:183], v[18:19], 0, v[178:179]
	s_and_b64 s[16:17], s[16:17], exec
	v_ashrrev_i32_e32 v21, 31, v20
	v_lshl_add_u64 v[22:23], v[182:183], 0, s[6:7]
	s_cselect_b32 s6, s53, s54
	v_lshlrev_b64 v[18:19], 8, v[20:21]
	v_add_u32_e32 v20, s52, v215
	v_add_u32_e32 v24, s6, v215
	v_ashrrev_i32_e32 v21, 31, v20
	v_ashrrev_i32_e32 v25, 31, v24
	v_lshl_add_u64 v[18:19], s[18:19], 0, v[18:19]
	v_lshlrev_b64 v[20:21], 8, v[20:21]
	v_lshlrev_b64 v[24:25], 8, v[24:25]
	v_lshl_add_u64 v[18:19], v[18:19], 0, v[178:179]
	v_lshl_add_u64 v[20:21], s[18:19], 0, v[20:21]
	v_lshl_add_u64 v[24:25], s[18:19], 0, v[24:25]
	global_load_dwordx2 v[26:27], v[22:23], off
	global_load_dwordx2 v[28:29], v[22:23], off offset:64
	s_nop 0
	global_load_dwordx2 v[22:23], v[22:23], off offset:128
	s_nop 0
	global_load_dwordx2 v[18:19], v[18:19], off
	v_lshl_add_u64 v[20:21], v[20:21], 0, v[178:179]
	v_lshl_add_u64 v[24:25], v[24:25], 0, v[178:179]
	global_load_dwordx2 v[20:21], v[20:21], off
	s_nop 0
	global_load_dwordx2 v[24:25], v[24:25], off
	s_nop 0
	s_nop 0
	s_nop 0
	v_cmp_eq_u32_e32 vcc, 0, v214
	v_lshlrev_b32_e32 v36, 5, v214
	s_cmp_lt_i32 s49, 4
	s_waitcnt vmcnt(9)
	v_lshlrev_b32_e32 v37, 16, v2
	v_and_b32_e32 v2, 0xffff0000, v2
	v_lshlrev_b32_e32 v39, 16, v4
	v_and_b32_e32 v4, 0xffff0000, v4
	s_waitcnt vmcnt(8)
	v_lshlrev_b32_e32 v41, 16, v6
	v_and_b32_e32 v6, 0xffff0000, v6
	v_cvt_pk_fp8_f32 v31, v37, v2
	v_cvt_pk_fp8_f32 v32, v39, v4
	v_cvt_pk_fp8_f32 v33, v41, v6
	v_lshlrev_b32_e32 v38, 16, v3
	v_and_b32_e32 v3, 0xffff0000, v3
	v_lshlrev_b32_e32 v40, 16, v5
	v_and_b32_e32 v5, 0xffff0000, v5
	v_lshlrev_b32_e32 v42, 16, v7
	v_and_b32_e32 v7, 0xffff0000, v7
	v_lshlrev_b32_e32 v43, 16, v8
	v_and_b32_e32 v2, 0xffff0000, v8
	v_cvt_pk_fp8_f32 v31, v38, v3 op_sel:[0,0,1]
	s_nop 0
	v_cvt_pk_fp8_f32 v32, v40, v5 op_sel:[0,0,1]
	v_cvt_pk_fp8_f32 v33, v42, v7 op_sel:[0,0,1]
	v_cvt_pk_fp8_f32 v3, v43, v2
	s_waitcnt vmcnt(7)
	v_lshlrev_b32_e32 v5, 16, v10
	v_and_b32_e32 v6, 0xffff0000, v10
	s_nop 0
	v_cvt_pk_fp8_f32 v7, v5, v6
	v_lshlrev_b32_e32 v2, 16, v9
	v_and_b32_e32 v4, 0xffff0000, v9
	v_cvt_pk_fp8_f32 v3, v2, v4 op_sel:[0,0,1]
	v_lshlrev_b32_e32 v2, 16, v11
	v_and_b32_e32 v4, 0xffff0000, v11
	v_cvt_pk_fp8_f32 v7, v2, v4 op_sel:[0,0,1]
	v_lshlrev_b32_e32 v2, 16, v12
	v_and_b32_e32 v4, 0xffff0000, v12
	s_nop 0
	v_cvt_pk_fp8_f32 v5, v2, v4
	s_waitcnt vmcnt(6)
	v_lshlrev_b32_e32 v6, 16, v14
	v_and_b32_e32 v8, 0xffff0000, v14
	s_nop 0
	v_cvt_pk_fp8_f32 v9, v6, v8
	v_lshlrev_b32_e32 v8, 16, v16
	v_and_b32_e32 v10, 0xffff0000, v16
	s_nop 0
	v_cvt_pk_fp8_f32 v11, v8, v10
	v_lshlrev_b32_e32 v2, 16, v13
	v_and_b32_e32 v4, 0xffff0000, v13
	v_lshlrev_b32_e32 v6, 16, v15
	v_and_b32_e32 v8, 0xffff0000, v15
	v_cvt_pk_fp8_f32 v5, v2, v4 op_sel:[0,0,1]
	v_lshlrev_b32_e32 v4, 2, v35
	v_lshlrev_b32_e32 v10, 16, v17
	v_and_b32_e32 v12, 0xffff0000, v17
	v_cvt_pk_fp8_f32 v9, v6, v8 op_sel:[0,0,1]
	v_mul_lo_u32 v2, v215, s38
	v_and_b32_e32 v6, 16, v4
	v_cvt_pk_fp8_f32 v11, v10, v12 op_sel:[0,0,1]
	v_add_u32_e32 v216, v2, v178
	v_add_u32_e32 v2, v2, v6
	v_and_or_b32 v217, v4, 12, v2
	v_add_u32_e32 v2, 0, v217
	v_cndmask_b32_e32 v117, 0, v3, vcc
	v_mul_u32_u24_e32 v8, 0x50, v30
	v_and_b32_e32 v125, v34, v3
	v_add_u32_e32 v3, 0, v216
	v_add_u32_e32 v4, 0x1400, v2
	v_cndmask_b32_e32 v121, 0, v11, vcc
	v_cndmask_b32_e32 v120, 0, v9, vcc
	v_cndmask_b32_e32 v119, 0, v5, vcc
	v_cndmask_b32_e32 v118, 0, v7, vcc
	v_cndmask_b32_e32 v116, 0, v33, vcc
	v_cndmask_b32_e32 v115, 0, v32, vcc
	v_cndmask_b32_e32 v114, 0, v31, vcc
	v_and_b32_e32 v129, v34, v11
	v_and_b32_e32 v128, v34, v9
	v_and_b32_e32 v127, v34, v5
	v_and_b32_e32 v126, v34, v7
	v_and_b32_e32 v124, v34, v33
	v_and_b32_e32 v123, v34, v32
	v_and_b32_e32 v122, v34, v31
	s_waitcnt vmcnt(2)
	ds_write_b64 v3, v[18:19]
	ds_write2_b32 v4, v26, v27 offset1:8
	s_waitcnt vmcnt(1)
	ds_write_b64 v3, v[20:21] offset:10240
	v_add_u32_e32 v4, 0x3c00, v2
	v_add_u32_e32 v2, 0x6400, v2
	v_add3_u32 v218, v36, v8, 0
	ds_write2_b32 v4, v28, v29 offset1:8
	s_waitcnt vmcnt(0)
	ds_write_b64 v3, v[24:25] offset:20480
	ds_write2_b32 v2, v22, v23 offset1:8
	s_waitcnt lgkmcnt(0)
	s_barrier
	ds_read_b128 v[2:5], v218
	ds_read_b128 v[6:9], v218 offset:16
	s_waitcnt lgkmcnt(0)
	v_mfma_f32_32x32x64_f8f6f4 v[82:97], v[2:9], v[114:121], 0
	v_mfma_f32_32x32x64_f8f6f4 v[66:81], v[2:9], v[122:129], 0
	s_cbranch_scc0 .LBB0_662
	s_setprio 1

; DI void attn_unit_d8(unsigned char* lds, const AttnArgs& a) {
;     ...
;     const int lane = tid & 63, r = lane & 31, h = lane >> 5; const int wid = __builtin_amdgcn_readfirstlane(tid >> 6);
;     v8i qfa, qfb;
;     { const bf16_t* qp = a.q + (size_t)(wid * 32 + r) * 256 + 32 * h;
;       const u32x4 q0 = *(const u32x4*)qp, q1 = *(const u32x4*)(qp + 8), q2 = *(const u32x4*)(qp + 16), q3 = *(const u32x4*)(qp + 24);
;       const u32x2 c0 = bf8_to_fp8(q0), c1 = bf8_to_fp8(q1), c2 = bf8_to_fp8(q2), c3 = bf8_to_fp8(q3);
;       const v8i qv = (v8i){(int)c0.x, (int)c0.y, (int)c1.x, (int)c1.y, (int)c2.x, (int)c2.y, (int)c3.x, (int)c3.y}, zz = (v8i){0, 0, 0, 0, 0, 0, 0, 0};
;       qfa = h == 0 ? qv : zz; qfb = h == 1 ? qv : zz; }
;     const int lrow = tid >> 3, lch = tid & 7;
;     const unsigned char* vsrc = a.vt8 + (size_t)lrow * KEYS + 8 * lch;
;     const int ldst = lrow * A8_PITCH + lch * 8;
;     const int ldv = A8_VOFF + lrow * A8_PITCH + (lch >> 2) * 16 + (lch & 3) * 4;
;     const int koff = r * A8_PITCH + 32 * h, voff = A8_VOFF + r * A8_PITCH + 32 * h;
;     f32x16 o0[2], o1[2];
; #pragma unroll
;     for (int d = 0; d < 2; ++d) { o0[d] = (f32x16){}; o1[d] = (f32x16){}; }
;     f32x4 l0 = {0.f, 0.f, 0.f, 0.f}, l1 = {0.f, 0.f, 0.f, 0.f};
;     constexpr int D8_SLOT = 2 * 64 * A8_PITCH;
;     u32x2 kreg0, vreg0, kreg1, vreg1;
;     auto gload = [&](int t, u32x2& kreg, u32x2& vreg) __attribute__((always_inline)) {
;         const unsigned char* kp = (t < 64) ? a.klat8 + (size_t)(t * 64 + lrow) * 256 : a.kctx8 + (size_t)((t - 64) * 64 + lrow) * 256;
;         kreg = *(const u32x2*)(kp + 8 * lch);
;         vreg = *(const u32x2*)(vsrc + (size_t)t * 64);
;     };
;     auto lstore = [&](int slot, const u32x2& kreg, const u32x2& vreg) __attribute__((always_inline)) { unsigned char* b = lds + slot * D8_SLOT;
;         *(u32x2*)(b + ldst) = kreg; *(unsigned*)(b + ldv) = vreg.x; *(unsigned*)(b + ldv + 32) = vreg.y; };
;     auto rd32 = [&](const unsigned char* p) __attribute__((always_inline)) -> v8i { const u32x4 lo = *(const u32x4*)p, hi = *(const u32x4*)(p + 16);
;         return (v8i){(int)lo.x, (int)lo.y, (int)lo.z, (int)lo.w, (int)hi.x, (int)hi.y, (int)hi.z, (int)hi.w}; };
;     auto expsum = [&](f32x16& sc, f32x4& l) __attribute__((always_inline)) {
; #pragma unroll
;         for (int i = 0; i < 16; ++i) sc[i] = __builtin_amdgcn_exp2f(sc[i]);
; #pragma unroll
.LBB0_1885:
	s_ashr_i32 s8, s46, 6
	s_lshl_b32 s16, s46, 8
	s_lshl_b32 s18, s8, 12
	s_and_b32 s16, s16, 0xf00
	s_or_b32 s16, s18, s16
	s_ashr_i32 s17, s16, 31
	s_lshl_b64 s[20:21], s[16:17], 9
	s_add_u32 s19, s4, s20
	s_addc_u32 s20, s5, s21
	s_lshl_b32 s21, s46, 2
	s_and_b32 s47, s21, 0xc0
	s_lshl_b32 s21, s47, 1
	s_add_u32 s50, s19, s21
	s_addc_u32 s51, s20, 0
	s_lshl_b32 s20, s8, 8
	s_ashr_i32 s19, s18, 31
	s_or_b32 s8, s20, s47
	s_lshl_b64 s[18:19], s[18:19], 8
	s_mul_hi_i32 s21, s8, 0x1100
	s_mulk_i32 s8, 0x1100
	s_add_u32 s22, s28, s8
	s_addc_u32 s23, s29, s21
	s_add_u32 s8, s24, s18
	s_addc_u32 s19, s25, s19
	v_mov_b32_e32 v18, v0
	s_add_u32 s18, s8, s47
	s_addc_u32 s19, s19, 0
	v_readfirstlane_b32 s8, v18
	v_and_b32_e32 v30, 31, v18
	s_ashr_i32 s8, s8, 6
	v_lshl_or_b32 v180, s8, 5, v30
	v_ashrrev_i32_e32 v181, 31, v180
	v_bfe_u32 v217, v18, 5, 1
	v_lshlrev_b64 v[2:3], 9, v[180:181]
	v_lshl_add_u64 v[2:3], s[50:51], 0, v[2:3]
	v_lshlrev_b32_e32 v178, 6, v217
	v_lshl_add_u64 v[14:15], v[2:3], 0, v[178:179]
	global_load_dwordx4 v[2:5], v[14:15], off
	global_load_dwordx4 v[6:9], v[14:15], off offset:16
	global_load_dwordx4 v[10:13], v[14:15], off offset:32
	s_nop 0
	global_load_dwordx4 v[14:17], v[14:15], off offset:48
	v_ashrrev_i32_e32 v182, 3, v18
	v_ashrrev_i32_e32 v183, 31, v182
	v_bfe_i32 v37, v18, 5, 1
	v_and_b32_e32 v38, 7, v18
	v_lshlrev_b64 v[18:19], 8, v[182:183]
	v_lshl_add_u64 v[18:19], s[18:19], 0, v[18:19]
	v_lshlrev_b32_e32 v178, 3, v38
	v_lshl_add_u64 v[18:19], v[18:19], 0, v[178:179]
	v_mov_b64_e32 v[20:21], s[22:23]
	v_add_co_u32_e32 v22, vcc, s39, v18
	v_mad_i64_i32 v[20:21], s[22:23], v182, s37, v[20:21]
	s_nop 0
	v_addc_co_u32_e32 v23, vcc, 0, v19, vcc
	v_lshl_add_u64 v[184:185], v[20:21], 0, v[178:179]
	global_load_dwordx2 v[20:21], v[18:19], off
	v_add_co_u32_e32 v18, vcc, s40, v18
	s_nop 0
	s_nop 0
	v_addc_co_u32_e32 v19, vcc, 0, v19, vcc
	global_load_dwordx2 v[24:25], v[184:185], off
	global_load_dwordx2 v[26:27], v[184:185], off offset:64
	global_load_dwordx2 v[28:29], v[184:185], off offset:128
	s_nop 0
	global_load_dwordx2 v[22:23], v[22:23], off
	s_nop 0
	global_load_dwordx2 v[18:19], v[18:19], off
	s_nop 0
	s_nop 0
	s_nop 0
	s_nop 0
	s_nop 0
	v_cmp_eq_u32_e32 vcc, 0, v217
	v_lshlrev_b32_e32 v39, 5, v217
	s_cmp_lt_i32 s8, 4
	s_waitcnt vmcnt(9)
	v_lshlrev_b32_e32 v40, 16, v2
	v_and_b32_e32 v2, 0xffff0000, v2
	v_lshlrev_b32_e32 v42, 16, v4
	v_and_b32_e32 v4, 0xffff0000, v4
	v_cvt_pk_fp8_f32 v31, v40, v2
	v_cvt_pk_fp8_f32 v32, v42, v4
	v_lshlrev_b32_e32 v41, 16, v3
	v_and_b32_e32 v3, 0xffff0000, v3
	v_lshlrev_b32_e32 v43, 16, v5
	v_and_b32_e32 v5, 0xffff0000, v5
	s_waitcnt vmcnt(8)
	v_lshlrev_b32_e32 v44, 16, v6
	v_and_b32_e32 v6, 0xffff0000, v6
	v_cvt_pk_fp8_f32 v31, v41, v3 op_sel:[0,0,1]
	s_waitcnt vmcnt(6)
	v_lshlrev_b32_e32 v2, 16, v14
	v_and_b32_e32 v3, 0xffff0000, v14
	s_nop 0
	v_cvt_pk_fp8_f32 v33, v44, v6
	v_cvt_pk_fp8_f32 v32, v43, v5 op_sel:[0,0,1]
	v_cvt_pk_fp8_f32 v4, v2, v3
	v_lshlrev_b32_e32 v3, 16, v16
	v_and_b32_e32 v5, 0xffff0000, v16
	s_nop 0
	v_lshlrev_b32_e32 v46, 16, v8
	v_and_b32_e32 v8, 0xffff0000, v8
	v_lshlrev_b32_e32 v48, 16, v10
	v_and_b32_e32 v10, 0xffff0000, v10
	v_lshlrev_b32_e32 v50, 16, v12
	v_and_b32_e32 v12, 0xffff0000, v12
	v_cvt_pk_fp8_f32 v6, v3, v5
	v_cvt_pk_fp8_f32 v34, v46, v8
	v_cvt_pk_fp8_f32 v35, v48, v10
	v_cvt_pk_fp8_f32 v36, v50, v12
	v_lshlrev_b32_e32 v45, 16, v7
	v_and_b32_e32 v7, 0xffff0000, v7
	v_lshlrev_b32_e32 v2, 16, v15
	v_and_b32_e32 v3, 0xffff0000, v15
	v_cvt_pk_fp8_f32 v33, v45, v7 op_sel:[0,0,1]
	v_lshlrev_b32_e32 v5, 16, v17
	v_and_b32_e32 v7, 0xffff0000, v17
	v_cvt_pk_fp8_f32 v4, v2, v3 op_sel:[0,0,1]
	v_lshlrev_b32_e32 v3, 2, v38
	v_lshlrev_b32_e32 v47, 16, v9
	v_and_b32_e32 v9, 0xffff0000, v9
	v_lshlrev_b32_e32 v49, 16, v11
	v_and_b32_e32 v11, 0xffff0000, v11
	v_lshlrev_b32_e32 v51, 16, v13
	v_and_b32_e32 v13, 0xffff0000, v13
	v_cvt_pk_fp8_f32 v6, v5, v7 op_sel:[0,0,1]
	v_mul_lo_u32 v2, v182, s38
	v_and_b32_e32 v5, 16, v3
	v_cvt_pk_fp8_f32 v34, v47, v9 op_sel:[0,0,1]
	v_cvt_pk_fp8_f32 v35, v49, v11 op_sel:[0,0,1]
	v_cvt_pk_fp8_f32 v36, v51, v13 op_sel:[0,0,1]
	v_add_u32_e32 v183, v2, v178
	v_add_u32_e32 v2, v2, v5
	v_and_or_b32 v218, v3, 12, v2
	v_add_u32_e32 v2, 0, v218
	v_cndmask_b32_e32 v120, 0, v4, vcc
	v_mul_u32_u24_e32 v7, 0x50, v30
	v_and_b32_e32 v128, v37, v4
	v_add_u32_e32 v4, 0, v183
	v_add_u32_e32 v3, 0x1400, v2
	v_cndmask_b32_e32 v121, 0, v6, vcc
	v_cndmask_b32_e32 v119, 0, v36, vcc
	v_cndmask_b32_e32 v118, 0, v35, vcc
	v_cndmask_b32_e32 v117, 0, v34, vcc
	v_cndmask_b32_e32 v116, 0, v33, vcc
	v_cndmask_b32_e32 v115, 0, v32, vcc
	v_cndmask_b32_e32 v114, 0, v31, vcc
	v_and_b32_e32 v129, v37, v6
	v_and_b32_e32 v127, v37, v36
	v_and_b32_e32 v126, v37, v35
	v_and_b32_e32 v125, v37, v34
	v_and_b32_e32 v124, v37, v33
	v_and_b32_e32 v123, v37, v32
	v_and_b32_e32 v122, v37, v31
	s_waitcnt vmcnt(5)
	ds_write_b64 v4, v[20:21]
	s_waitcnt vmcnt(4)
	ds_write2_b32 v3, v24, v25 offset1:8
	s_waitcnt vmcnt(1)
	ds_write_b64 v4, v[22:23] offset:10240
	v_add_u32_e32 v3, 0x3c00, v2
	v_add_u32_e32 v2, 0x6400, v2
	v_add3_u32 v219, v39, v7, 0
	ds_write2_b32 v3, v26, v27 offset1:8
	s_waitcnt vmcnt(0)
	ds_write_b64 v4, v[18:19] offset:20480
	ds_write2_b32 v2, v28, v29 offset1:8
	s_waitcnt lgkmcnt(0)
	s_barrier
	ds_read_b128 v[2:5], v219
	ds_read_b128 v[6:9], v219 offset:16
	s_waitcnt lgkmcnt(0)
	v_mfma_f32_32x32x64_f8f6f4 v[82:97], v[2:9], v[114:121], 0
	v_mfma_f32_32x32x64_f8f6f4 v[66:81], v[2:9], v[122:129], 0
	s_cbranch_scc0 .LBB0_1887
	s_setprio 1
